# grid barrier: non-leaders poll the global release word directly (one relay hop less)
# baseline (speedup 1.0000x reference)
.LBB0_116:
	v_readlane_b32 s2, v255, 21
	s_lshl_b32 s2, s2, 8
	v_readlane_b32 s4, v255, 19
	v_readlane_b32 s5, v255, 20
	s_add_u32 s2, s4, s2
	s_addc_u32 s3, s5, 0
	v_mov_b32_e32 v2, 0x1000
	v_mov_b32_e32 v4, 1
	global_atomic_add v4, v2, v4, s[2:3] offset:1024 sc0
	v_cvt_f32_u32_e32 v2, v3
	v_sub_u32_e32 v5, 0, v3
	v_rcp_iflag_f32_e32 v2, v2
	s_nop 0
	v_mul_f32_e32 v2, 0x4f7ffffe, v2
	v_cvt_u32_f32_e32 v2, v2
	v_mul_lo_u32 v5, v5, v2
	v_mul_hi_u32 v5, v2, v5
	v_add_u32_e32 v2, v2, v5
	s_waitcnt vmcnt(0)
	v_mul_hi_u32 v2, v4, v2
	v_mul_lo_u32 v5, v2, v3
	v_sub_u32_e32 v5, v4, v5
	v_add_u32_e32 v6, 1, v2
	v_cmp_ge_u32_e32 vcc, v5, v3
	v_add_u32_e32 v4, 1, v4
	s_nop 0
	v_cndmask_b32_e32 v2, v2, v6, vcc
	v_sub_u32_e32 v6, v5, v3
	v_cndmask_b32_e32 v5, v5, v6, vcc
	v_add_u32_e32 v6, 1, v2
	v_cmp_ge_u32_e32 vcc, v5, v3
	s_nop 1
	v_cndmask_b32_e32 v2, v2, v6, vcc
	v_mul_lo_u32 v5, v3, v2
	v_add_u32_e32 v3, v5, v3
	v_cmp_ne_u32_e32 vcc, v4, v3
	s_and_saveexec_b64 s[4:5], vcc
	s_xor_b64 s[4:5], exec, s[4:5]
	s_cbranch_execz .LBB0_130
	s_waitcnt lgkmcnt(0)
	v_mov_b32_e32 v1, 0x7500
	global_load_dword v1, v1, s[92:93] sc1
	s_add_u32 s10, s92, 0x7500
	s_addc_u32 s11, s93, 0
	s_waitcnt vmcnt(0)
	v_cmp_eq_u32_e32 vcc, v1, v2
	s_and_saveexec_b64 s[6:7], vcc
	s_cbranch_execz .LBB0_129
	s_add_u32 s8, s92, 0x4200
	s_addc_u32 s9, s93, 0
	s_mov_b32 s22, 1
	s_mov_b64 s[12:13], 0
	v_mov_b32_e32 v1, 0
	s_branch .LBB0_120
